# priority: per-segment s_setprio toggles removed from the four GEMM K-loops (64 instructions), waves keep their entry priority
# baseline (speedup 1.0000x reference)
.LBB0_310:
	v_add_u32_e32 v64, s34, v185
	ds_read_b128 v[130:133], v64
	ds_read_b128 v[134:137], v64 offset:1024
	ds_read_b128 v[138:141], v64 offset:2048
	ds_read_b128 v[142:145], v64 offset:3072
	v_add_u32_e32 v64, s37, v185
	ds_read_b128 v[158:161], v64
	ds_read_b128 v[162:165], v64 offset:1024
	ds_read_b128 v[166:169], v64 offset:2048
	ds_read_b128 v[170:173], v64 offset:3072
	s_add_u32 s26, s24, 0xfffc0080
	s_addc_u32 s27, s25, -1
	s_cmp_eq_u32 s56, 12
	s_cselect_b32 s29, s19, s27
	s_cselect_b32 s28, s33, s26
	s_cselect_b32 s27, s17, s55
	s_cselect_b32 s26, s53, s54
	s_add_i32 m0, s40, 0xc000
	ds_read_b128 v[174:177], v188
	ds_read_b128 v[178:181], v188 offset:1024
	ds_read_b128 v[190:193], v188 offset:2048
	ds_read_b128 v[212:215], v188 offset:3072
	ds_read_b128 v[216:219], v188 offset:4096
	ds_read_b128 v[220:223], v188 offset:5120
	ds_read_b128 v[224:227], v188 offset:6144
	ds_read_b128 v[228:231], v188 offset:7168
	global_load_lds_dwordx4 v154, s[24:25]
	s_add_i32 m0, s40, 0xe000
	s_nop 0
	global_load_lds_dwordx4 v156, s[24:25]
	s_waitcnt vmcnt(8)
	s_waitcnt lgkmcnt(0)
	s_barrier
	s_waitcnt lgkmcnt(0)
	v_mfma_f32_16x16x32_bf16 v[126:129], v[130:133], v[174:177], v[126:129]
	v_mfma_f32_16x16x32_bf16 v[122:125], v[138:141], v[174:177], v[122:125]
	v_mfma_f32_16x16x32_bf16 v[118:121], v[130:133], v[190:193], v[118:121]
	v_mfma_f32_16x16x32_bf16 v[110:113], v[138:141], v[190:193], v[110:113]
	v_mfma_f32_16x16x32_bf16 v[102:105], v[130:133], v[216:219], v[102:105]
	v_mfma_f32_16x16x32_bf16 v[94:97], v[138:141], v[216:219], v[94:97]
	v_mfma_f32_16x16x32_bf16 v[86:89], v[130:133], v[224:227], v[86:89]
	v_mfma_f32_16x16x32_bf16 v[78:81], v[138:141], v[224:227], v[78:81]
	v_mfma_f32_16x16x32_bf16 v[126:129], v[134:137], v[178:181], v[126:129]
	v_mfma_f32_16x16x32_bf16 v[122:125], v[142:145], v[178:181], v[122:125]
	v_mfma_f32_16x16x32_bf16 v[118:121], v[134:137], v[212:215], v[118:121]
	v_mfma_f32_16x16x32_bf16 v[110:113], v[142:145], v[212:215], v[110:113]
	v_mfma_f32_16x16x32_bf16 v[102:105], v[134:137], v[220:223], v[102:105]
	v_mfma_f32_16x16x32_bf16 v[94:97], v[142:145], v[220:223], v[94:97]
	v_mfma_f32_16x16x32_bf16 v[86:89], v[134:137], v[228:231], v[86:89]
	v_mfma_f32_16x16x32_bf16 v[78:81], v[142:145], v[228:231], v[78:81]
	v_mfma_f32_16x16x32_bf16 v[114:117], v[158:161], v[174:177], v[114:117]
	v_mfma_f32_16x16x32_bf16 v[106:109], v[166:169], v[174:177], v[106:109]
	v_mfma_f32_16x16x32_bf16 v[98:101], v[158:161], v[190:193], v[98:101]
	v_mfma_f32_16x16x32_bf16 v[90:93], v[166:169], v[190:193], v[90:93]
	v_mfma_f32_16x16x32_bf16 v[82:85], v[158:161], v[216:219], v[82:85]
	v_mfma_f32_16x16x32_bf16 v[74:77], v[166:169], v[216:219], v[74:77]
	v_mfma_f32_16x16x32_bf16 v[70:73], v[158:161], v[224:227], v[70:73]
	v_mfma_f32_16x16x32_bf16 v[66:69], v[166:169], v[224:227], v[66:69]
	v_mfma_f32_16x16x32_bf16 v[114:117], v[162:165], v[178:181], v[114:117]
	v_mfma_f32_16x16x32_bf16 v[106:109], v[170:173], v[178:181], v[106:109]
	v_mfma_f32_16x16x32_bf16 v[98:101], v[162:165], v[212:215], v[98:101]
	v_mfma_f32_16x16x32_bf16 v[90:93], v[170:173], v[212:215], v[90:93]
	v_mfma_f32_16x16x32_bf16 v[82:85], v[162:165], v[220:223], v[82:85]
	v_mfma_f32_16x16x32_bf16 v[74:77], v[170:173], v[220:223], v[74:77]
	v_mfma_f32_16x16x32_bf16 v[70:73], v[162:165], v[228:231], v[70:73]
	v_mfma_f32_16x16x32_bf16 v[66:69], v[170:173], v[228:231], v[66:69]
	s_barrier
	s_mov_b32 m0, s35
	s_add_u32 s58, s26, 0x40000
	ds_read_b128 v[174:177], v188 offset:16384
	ds_read_b128 v[178:181], v188 offset:17408
	ds_read_b128 v[190:193], v188 offset:18432
	ds_read_b128 v[212:215], v188 offset:19456
	ds_read_b128 v[216:219], v188 offset:20480
	ds_read_b128 v[220:223], v188 offset:21504
	ds_read_b128 v[224:227], v188 offset:22528
	ds_read_b128 v[228:231], v188 offset:23552
	global_load_lds_dwordx4 v150, s[26:27]
	s_mov_b32 m0, s36
	s_addc_u32 s59, s27, 0
	global_load_lds_dwordx4 v146, s[26:27]
	s_mov_b32 m0, s38
	s_nop 0
	global_load_lds_dwordx4 v150, s[58:59]
	s_mov_b32 m0, s39
	s_nop 0
	global_load_lds_dwordx4 v146, s[58:59]
	s_mov_b32 m0, s40
	s_nop 0
	global_load_lds_dwordx4 v152, s[28:29]
	s_mov_b32 m0, s41
	s_nop 0
	global_load_lds_dwordx4 v148, s[28:29]
	s_waitcnt vmcnt(8)
	s_waitcnt lgkmcnt(0)
	s_barrier
	s_waitcnt lgkmcnt(0)
	v_mfma_f32_16x16x32_bf16 v[60:63], v[130:133], v[174:177], v[60:63]
	v_mfma_f32_16x16x32_bf16 v[56:59], v[138:141], v[174:177], v[56:59]
	v_mfma_f32_16x16x32_bf16 v[52:55], v[130:133], v[190:193], v[52:55]
	v_mfma_f32_16x16x32_bf16 v[44:47], v[138:141], v[190:193], v[44:47]
	v_mfma_f32_16x16x32_bf16 v[36:39], v[130:133], v[216:219], v[36:39]
	v_mfma_f32_16x16x32_bf16 v[28:31], v[138:141], v[216:219], v[28:31]
	v_mfma_f32_16x16x32_bf16 v[20:23], v[130:133], v[224:227], v[20:23]
	v_mfma_f32_16x16x32_bf16 v[12:15], v[138:141], v[224:227], v[12:15]
	v_mfma_f32_16x16x32_bf16 v[60:63], v[134:137], v[178:181], v[60:63]
	v_mfma_f32_16x16x32_bf16 v[56:59], v[142:145], v[178:181], v[56:59]
	v_mfma_f32_16x16x32_bf16 v[52:55], v[134:137], v[212:215], v[52:55]
	v_mfma_f32_16x16x32_bf16 v[44:47], v[142:145], v[212:215], v[44:47]
	v_mfma_f32_16x16x32_bf16 v[36:39], v[134:137], v[220:223], v[36:39]
	v_mfma_f32_16x16x32_bf16 v[28:31], v[142:145], v[220:223], v[28:31]
	v_mfma_f32_16x16x32_bf16 v[20:23], v[134:137], v[228:231], v[20:23]
	v_mfma_f32_16x16x32_bf16 v[12:15], v[142:145], v[228:231], v[12:15]
	v_mfma_f32_16x16x32_bf16 v[48:51], v[158:161], v[174:177], v[48:51]
	v_mfma_f32_16x16x32_bf16 v[40:43], v[166:169], v[174:177], v[40:43]
	v_mfma_f32_16x16x32_bf16 v[32:35], v[158:161], v[190:193], v[32:35]
	v_mfma_f32_16x16x32_bf16 v[24:27], v[166:169], v[190:193], v[24:27]
	v_mfma_f32_16x16x32_bf16 v[16:19], v[158:161], v[216:219], v[16:19]
	v_mfma_f32_16x16x32_bf16 v[8:11], v[166:169], v[216:219], v[8:11]
	v_mfma_f32_16x16x32_bf16 v[4:7], v[158:161], v[224:227], v[4:7]
	v_mfma_f32_16x16x32_bf16 v[0:3], v[166:169], v[224:227], v[0:3]
	v_mfma_f32_16x16x32_bf16 v[48:51], v[162:165], v[178:181], v[48:51]
	v_mfma_f32_16x16x32_bf16 v[40:43], v[170:173], v[178:181], v[40:43]
	v_mfma_f32_16x16x32_bf16 v[32:35], v[162:165], v[212:215], v[32:35]
	v_mfma_f32_16x16x32_bf16 v[24:27], v[170:173], v[212:215], v[24:27]
	v_mfma_f32_16x16x32_bf16 v[16:19], v[162:165], v[220:223], v[16:19]
	v_mfma_f32_16x16x32_bf16 v[8:11], v[170:173], v[220:223], v[8:11]
	v_mfma_f32_16x16x32_bf16 v[4:7], v[162:165], v[228:231], v[4:7]
	v_mfma_f32_16x16x32_bf16 v[0:3], v[170:173], v[228:231], v[0:3]
	s_barrier
	v_add_u32_e32 v64, s44, v185
	ds_read_b128 v[130:133], v64
	ds_read_b128 v[134:137], v64 offset:1024
	ds_read_b128 v[138:141], v64 offset:2048
	ds_read_b128 v[142:145], v64 offset:3072
	v_add_u32_e32 v64, s49, v185
	ds_read_b128 v[158:161], v64
	ds_read_b128 v[162:165], v64 offset:1024
	ds_read_b128 v[166:169], v64 offset:2048
	ds_read_b128 v[170:173], v64 offset:3072
	s_add_u32 s28, s28, 0x40000
	s_addc_u32 s29, s29, 0
	s_mov_b32 m0, s42
	ds_read_b128 v[174:177], v188 offset:32768
	ds_read_b128 v[178:181], v188 offset:33792
	ds_read_b128 v[190:193], v188 offset:34816
	ds_read_b128 v[212:215], v188 offset:35840
	ds_read_b128 v[216:219], v188 offset:36864
	ds_read_b128 v[220:223], v188 offset:37888
	ds_read_b128 v[224:227], v188 offset:38912
	ds_read_b128 v[228:231], v188 offset:39936
	global_load_lds_dwordx4 v152, s[28:29]
	s_mov_b32 m0, s43
	s_nop 0
	global_load_lds_dwordx4 v148, s[28:29]
	s_waitcnt vmcnt(8)
	s_waitcnt lgkmcnt(0)
	s_barrier
	s_waitcnt lgkmcnt(0)
	v_mfma_f32_16x16x32_bf16 v[126:129], v[130:133], v[174:177], v[126:129]
	v_mfma_f32_16x16x32_bf16 v[122:125], v[138:141], v[174:177], v[122:125]
	v_mfma_f32_16x16x32_bf16 v[118:121], v[130:133], v[190:193], v[118:121]
	v_mfma_f32_16x16x32_bf16 v[110:113], v[138:141], v[190:193], v[110:113]
	v_mfma_f32_16x16x32_bf16 v[102:105], v[130:133], v[216:219], v[102:105]
	v_mfma_f32_16x16x32_bf16 v[94:97], v[138:141], v[216:219], v[94:97]
	v_mfma_f32_16x16x32_bf16 v[86:89], v[130:133], v[224:227], v[86:89]
	v_mfma_f32_16x16x32_bf16 v[78:81], v[138:141], v[224:227], v[78:81]
	v_mfma_f32_16x16x32_bf16 v[126:129], v[134:137], v[178:181], v[126:129]
	v_mfma_f32_16x16x32_bf16 v[122:125], v[142:145], v[178:181], v[122:125]
	v_mfma_f32_16x16x32_bf16 v[118:121], v[134:137], v[212:215], v[118:121]
	v_mfma_f32_16x16x32_bf16 v[110:113], v[142:145], v[212:215], v[110:113]
	v_mfma_f32_16x16x32_bf16 v[102:105], v[134:137], v[220:223], v[102:105]
	v_mfma_f32_16x16x32_bf16 v[94:97], v[142:145], v[220:223], v[94:97]
	v_mfma_f32_16x16x32_bf16 v[86:89], v[134:137], v[228:231], v[86:89]
	v_mfma_f32_16x16x32_bf16 v[78:81], v[142:145], v[228:231], v[78:81]
	v_mfma_f32_16x16x32_bf16 v[114:117], v[158:161], v[174:177], v[114:117]
	v_mfma_f32_16x16x32_bf16 v[106:109], v[166:169], v[174:177], v[106:109]
	v_mfma_f32_16x16x32_bf16 v[98:101], v[158:161], v[190:193], v[98:101]
	v_mfma_f32_16x16x32_bf16 v[90:93], v[166:169], v[190:193], v[90:93]
	v_mfma_f32_16x16x32_bf16 v[82:85], v[158:161], v[216:219], v[82:85]
	v_mfma_f32_16x16x32_bf16 v[74:77], v[166:169], v[216:219], v[74:77]
	v_mfma_f32_16x16x32_bf16 v[70:73], v[158:161], v[224:227], v[70:73]
	v_mfma_f32_16x16x32_bf16 v[66:69], v[166:169], v[224:227], v[66:69]
	v_mfma_f32_16x16x32_bf16 v[114:117], v[162:165], v[178:181], v[114:117]
	v_mfma_f32_16x16x32_bf16 v[106:109], v[170:173], v[178:181], v[106:109]
	v_mfma_f32_16x16x32_bf16 v[98:101], v[162:165], v[212:215], v[98:101]
	v_mfma_f32_16x16x32_bf16 v[90:93], v[170:173], v[212:215], v[90:93]
	v_mfma_f32_16x16x32_bf16 v[82:85], v[162:165], v[220:223], v[82:85]
	v_mfma_f32_16x16x32_bf16 v[74:77], v[170:173], v[220:223], v[74:77]
	v_mfma_f32_16x16x32_bf16 v[70:73], v[162:165], v[228:231], v[70:73]
	v_mfma_f32_16x16x32_bf16 v[66:69], v[170:173], v[228:231], v[66:69]
	s_barrier
	s_mov_b32 m0, s45
	s_add_u32 s100, s26, s68
	s_addc_u32 s101, s27, s69
	s_add_u32 s26, s26, 0x40080
	ds_read_b128 v[174:177], v188 offset:49152
	ds_read_b128 v[178:181], v188 offset:50176
	ds_read_b128 v[190:193], v188 offset:51200
	ds_read_b128 v[212:215], v188 offset:52224
	ds_read_b128 v[216:219], v188 offset:53248
	ds_read_b128 v[220:223], v188 offset:54272
	ds_read_b128 v[224:227], v188 offset:55296
	ds_read_b128 v[228:231], v188 offset:56320
	global_load_lds_dwordx4 v150, s[100:101]
	s_mov_b32 m0, s46
	s_addc_u32 s27, s27, 0
	global_load_lds_dwordx4 v146, s[100:101]
	s_mov_b32 m0, s50
	s_add_u32 s100, s28, s68
	global_load_lds_dwordx4 v150, s[26:27]
	s_addc_u32 s101, s29, s69
	s_mov_b32 m0, s51
	s_sub_u32 s100, s100, 0x40000
	global_load_lds_dwordx4 v146, s[26:27]
	s_subb_u32 s101, s101, 0
	s_mov_b32 m0, s47
	s_nop 0
	global_load_lds_dwordx4 v152, s[100:101]
	s_mov_b32 m0, s48
	s_nop 0
	global_load_lds_dwordx4 v148, s[100:101]
	s_waitcnt vmcnt(8)
	s_waitcnt lgkmcnt(0)
	s_barrier
	s_waitcnt lgkmcnt(0)
	v_mfma_f32_16x16x32_bf16 v[60:63], v[130:133], v[174:177], v[60:63]
	v_mfma_f32_16x16x32_bf16 v[56:59], v[138:141], v[174:177], v[56:59]
	v_mfma_f32_16x16x32_bf16 v[52:55], v[130:133], v[190:193], v[52:55]
	v_mfma_f32_16x16x32_bf16 v[44:47], v[138:141], v[190:193], v[44:47]
	v_mfma_f32_16x16x32_bf16 v[36:39], v[130:133], v[216:219], v[36:39]
	v_mfma_f32_16x16x32_bf16 v[28:31], v[138:141], v[216:219], v[28:31]
	v_mfma_f32_16x16x32_bf16 v[20:23], v[130:133], v[224:227], v[20:23]
	v_mfma_f32_16x16x32_bf16 v[12:15], v[138:141], v[224:227], v[12:15]
	v_mfma_f32_16x16x32_bf16 v[60:63], v[134:137], v[178:181], v[60:63]
	v_mfma_f32_16x16x32_bf16 v[56:59], v[142:145], v[178:181], v[56:59]
	v_mfma_f32_16x16x32_bf16 v[52:55], v[134:137], v[212:215], v[52:55]
	v_mfma_f32_16x16x32_bf16 v[44:47], v[142:145], v[212:215], v[44:47]
	v_mfma_f32_16x16x32_bf16 v[36:39], v[134:137], v[220:223], v[36:39]
	v_mfma_f32_16x16x32_bf16 v[28:31], v[142:145], v[220:223], v[28:31]
	v_mfma_f32_16x16x32_bf16 v[20:23], v[134:137], v[228:231], v[20:23]
	v_mfma_f32_16x16x32_bf16 v[12:15], v[142:145], v[228:231], v[12:15]
	v_mfma_f32_16x16x32_bf16 v[48:51], v[158:161], v[174:177], v[48:51]
	v_mfma_f32_16x16x32_bf16 v[40:43], v[166:169], v[174:177], v[40:43]
	v_mfma_f32_16x16x32_bf16 v[32:35], v[158:161], v[190:193], v[32:35]
	v_mfma_f32_16x16x32_bf16 v[24:27], v[166:169], v[190:193], v[24:27]
	v_mfma_f32_16x16x32_bf16 v[16:19], v[158:161], v[216:219], v[16:19]
	v_mfma_f32_16x16x32_bf16 v[8:11], v[166:169], v[216:219], v[8:11]
	v_mfma_f32_16x16x32_bf16 v[4:7], v[158:161], v[224:227], v[4:7]
	v_mfma_f32_16x16x32_bf16 v[0:3], v[166:169], v[224:227], v[0:3]
	v_mfma_f32_16x16x32_bf16 v[48:51], v[162:165], v[178:181], v[48:51]
	v_mfma_f32_16x16x32_bf16 v[40:43], v[170:173], v[178:181], v[40:43]
	v_mfma_f32_16x16x32_bf16 v[32:35], v[162:165], v[212:215], v[32:35]
	v_mfma_f32_16x16x32_bf16 v[24:27], v[170:173], v[212:215], v[24:27]
	v_mfma_f32_16x16x32_bf16 v[16:19], v[162:165], v[220:223], v[16:19]
	v_mfma_f32_16x16x32_bf16 v[8:11], v[170:173], v[220:223], v[8:11]
	v_mfma_f32_16x16x32_bf16 v[4:7], v[162:165], v[228:231], v[4:7]
	v_mfma_f32_16x16x32_bf16 v[0:3], v[170:173], v[228:231], v[0:3]
	s_barrier
	s_add_i32 s56, s56, 2
	s_add_u32 s24, s24, 0x100
	s_addc_u32 s25, s25, 0
	s_add_u32 s54, s54, 0x100
	s_addc_u32 s55, s55, 0
	s_cmp_gt_u32 s56, 13
	s_cbranch_scc0 .LBB0_310
	s_and_b64 vcc, exec, s[14:15]
	s_cbranch_vccz .LBB0_313
	s_barrier

.LBB0_814:
	v_add_u32_e32 v64, s11, v173
	ds_read_b128 v[66:69], v64
	ds_read_b128 v[70:73], v64 offset:1024
	ds_read_b128 v[74:77], v64 offset:2048
	ds_read_b128 v[78:81], v64 offset:3072
	v_add_u32_e32 v64, s34, v173
	ds_read_b128 v[146:149], v64
	ds_read_b128 v[150:153], v64 offset:1024
	ds_read_b128 v[166:169], v64 offset:2048
	ds_read_b128 v[176:179], v64 offset:3072
	s_add_u32 s4, s0, 0xfffc0080
	s_addc_u32 s5, s1, -1
	s_cmp_eq_u32 s61, 12
	s_cselect_b32 s27, s55, s5
	s_cselect_b32 s26, s56, s4
	s_cselect_b32 s5, s57, s60
	s_cselect_b32 s4, s58, s59
	s_add_i32 m0, s37, 0xc000
	ds_read_b128 v[180:183], v175
	ds_read_b128 v[184:187], v175 offset:1024
	ds_read_b128 v[188:191], v175 offset:2048
	ds_read_b128 v[192:195], v175 offset:3072
	ds_read_b128 v[212:215], v175 offset:4096
	ds_read_b128 v[216:219], v175 offset:5120
	ds_read_b128 v[220:223], v175 offset:6144
	ds_read_b128 v[224:227], v175 offset:7168
	global_load_lds_dwordx4 v162, s[0:1]
	s_add_i32 m0, s37, 0xe000
	s_nop 0
	global_load_lds_dwordx4 v164, s[0:1]
	s_waitcnt vmcnt(8)
	s_waitcnt lgkmcnt(0)
	s_barrier
	s_waitcnt lgkmcnt(0)
	v_mfma_f32_16x16x32_bf16 v[142:145], v[66:69], v[180:183], v[142:145]
	v_mfma_f32_16x16x32_bf16 v[138:141], v[74:77], v[180:183], v[138:141]
	v_mfma_f32_16x16x32_bf16 v[126:129], v[66:69], v[188:191], v[126:129]
	v_mfma_f32_16x16x32_bf16 v[122:125], v[74:77], v[188:191], v[122:125]
	v_mfma_f32_16x16x32_bf16 v[110:113], v[66:69], v[212:215], v[110:113]
	v_mfma_f32_16x16x32_bf16 v[106:109], v[74:77], v[212:215], v[106:109]
	v_mfma_f32_16x16x32_bf16 v[94:97], v[66:69], v[220:223], v[94:97]
	v_mfma_f32_16x16x32_bf16 v[90:93], v[74:77], v[220:223], v[90:93]
	v_mfma_f32_16x16x32_bf16 v[142:145], v[70:73], v[184:187], v[142:145]
	v_mfma_f32_16x16x32_bf16 v[138:141], v[78:81], v[184:187], v[138:141]
	v_mfma_f32_16x16x32_bf16 v[126:129], v[70:73], v[192:195], v[126:129]
	v_mfma_f32_16x16x32_bf16 v[122:125], v[78:81], v[192:195], v[122:125]
	v_mfma_f32_16x16x32_bf16 v[110:113], v[70:73], v[216:219], v[110:113]
	v_mfma_f32_16x16x32_bf16 v[106:109], v[78:81], v[216:219], v[106:109]
	v_mfma_f32_16x16x32_bf16 v[94:97], v[70:73], v[224:227], v[94:97]
	v_mfma_f32_16x16x32_bf16 v[90:93], v[78:81], v[224:227], v[90:93]
	v_mfma_f32_16x16x32_bf16 v[134:137], v[146:149], v[180:183], v[134:137]
	v_mfma_f32_16x16x32_bf16 v[130:133], v[166:169], v[180:183], v[130:133]
	v_mfma_f32_16x16x32_bf16 v[118:121], v[146:149], v[188:191], v[118:121]
	v_mfma_f32_16x16x32_bf16 v[114:117], v[166:169], v[188:191], v[114:117]
	v_mfma_f32_16x16x32_bf16 v[102:105], v[146:149], v[212:215], v[102:105]
	v_mfma_f32_16x16x32_bf16 v[98:101], v[166:169], v[212:215], v[98:101]
	v_mfma_f32_16x16x32_bf16 v[86:89], v[146:149], v[220:223], v[86:89]
	v_mfma_f32_16x16x32_bf16 v[82:85], v[166:169], v[220:223], v[82:85]
	v_mfma_f32_16x16x32_bf16 v[134:137], v[150:153], v[184:187], v[134:137]
	v_mfma_f32_16x16x32_bf16 v[130:133], v[176:179], v[184:187], v[130:133]
	v_mfma_f32_16x16x32_bf16 v[118:121], v[150:153], v[192:195], v[118:121]
	v_mfma_f32_16x16x32_bf16 v[114:117], v[176:179], v[192:195], v[114:117]
	v_mfma_f32_16x16x32_bf16 v[102:105], v[150:153], v[216:219], v[102:105]
	v_mfma_f32_16x16x32_bf16 v[98:101], v[176:179], v[216:219], v[98:101]
	v_mfma_f32_16x16x32_bf16 v[86:89], v[150:153], v[224:227], v[86:89]
	v_mfma_f32_16x16x32_bf16 v[82:85], v[176:179], v[224:227], v[82:85]
	s_barrier
	s_mov_b32 m0, s31
	s_add_u32 s62, s4, 0x40000
	ds_read_b128 v[180:183], v175 offset:16384
	ds_read_b128 v[184:187], v175 offset:17408
	ds_read_b128 v[188:191], v175 offset:18432
	ds_read_b128 v[192:195], v175 offset:19456
	ds_read_b128 v[212:215], v175 offset:20480
	ds_read_b128 v[216:219], v175 offset:21504
	ds_read_b128 v[220:223], v175 offset:22528
	ds_read_b128 v[224:227], v175 offset:23552
	global_load_lds_dwordx4 v158, s[4:5]
	s_mov_b32 m0, s33
	s_addc_u32 s63, s5, 0
	global_load_lds_dwordx4 v154, s[4:5]
	s_mov_b32 m0, s35
	s_nop 0
	global_load_lds_dwordx4 v158, s[62:63]
	s_mov_b32 m0, s36
	s_nop 0
	global_load_lds_dwordx4 v154, s[62:63]
	s_mov_b32 m0, s37
	s_nop 0
	global_load_lds_dwordx4 v160, s[26:27]
	s_mov_b32 m0, s38
	s_nop 0
	global_load_lds_dwordx4 v156, s[26:27]
	s_waitcnt vmcnt(8)
	s_waitcnt lgkmcnt(0)
	s_barrier
	s_waitcnt lgkmcnt(0)
	v_mfma_f32_16x16x32_bf16 v[60:63], v[66:69], v[180:183], v[60:63]
	v_mfma_f32_16x16x32_bf16 v[56:59], v[74:77], v[180:183], v[56:59]
	v_mfma_f32_16x16x32_bf16 v[44:47], v[66:69], v[188:191], v[44:47]
	v_mfma_f32_16x16x32_bf16 v[40:43], v[74:77], v[188:191], v[40:43]
	v_mfma_f32_16x16x32_bf16 v[28:31], v[66:69], v[212:215], v[28:31]
	v_mfma_f32_16x16x32_bf16 v[24:27], v[74:77], v[212:215], v[24:27]
	v_mfma_f32_16x16x32_bf16 v[12:15], v[66:69], v[220:223], v[12:15]
	v_mfma_f32_16x16x32_bf16 v[8:11], v[74:77], v[220:223], v[8:11]
	v_mfma_f32_16x16x32_bf16 v[60:63], v[70:73], v[184:187], v[60:63]
	v_mfma_f32_16x16x32_bf16 v[56:59], v[78:81], v[184:187], v[56:59]
	v_mfma_f32_16x16x32_bf16 v[44:47], v[70:73], v[192:195], v[44:47]
	v_mfma_f32_16x16x32_bf16 v[40:43], v[78:81], v[192:195], v[40:43]
	v_mfma_f32_16x16x32_bf16 v[28:31], v[70:73], v[216:219], v[28:31]
	v_mfma_f32_16x16x32_bf16 v[24:27], v[78:81], v[216:219], v[24:27]
	v_mfma_f32_16x16x32_bf16 v[12:15], v[70:73], v[224:227], v[12:15]
	v_mfma_f32_16x16x32_bf16 v[8:11], v[78:81], v[224:227], v[8:11]
	v_mfma_f32_16x16x32_bf16 v[52:55], v[146:149], v[180:183], v[52:55]
	v_mfma_f32_16x16x32_bf16 v[48:51], v[166:169], v[180:183], v[48:51]
	v_mfma_f32_16x16x32_bf16 v[36:39], v[146:149], v[188:191], v[36:39]
	v_mfma_f32_16x16x32_bf16 v[32:35], v[166:169], v[188:191], v[32:35]
	v_mfma_f32_16x16x32_bf16 v[20:23], v[146:149], v[212:215], v[20:23]
	v_mfma_f32_16x16x32_bf16 v[16:19], v[166:169], v[212:215], v[16:19]
	v_mfma_f32_16x16x32_bf16 v[4:7], v[146:149], v[220:223], v[4:7]
	v_mfma_f32_16x16x32_bf16 v[0:3], v[166:169], v[220:223], v[0:3]
	v_mfma_f32_16x16x32_bf16 v[52:55], v[150:153], v[184:187], v[52:55]
	v_mfma_f32_16x16x32_bf16 v[48:51], v[176:179], v[184:187], v[48:51]
	v_mfma_f32_16x16x32_bf16 v[36:39], v[150:153], v[192:195], v[36:39]
	v_mfma_f32_16x16x32_bf16 v[32:35], v[176:179], v[192:195], v[32:35]
	v_mfma_f32_16x16x32_bf16 v[20:23], v[150:153], v[216:219], v[20:23]
	v_mfma_f32_16x16x32_bf16 v[16:19], v[176:179], v[216:219], v[16:19]
	v_mfma_f32_16x16x32_bf16 v[4:7], v[150:153], v[224:227], v[4:7]
	v_mfma_f32_16x16x32_bf16 v[0:3], v[176:179], v[224:227], v[0:3]
	s_barrier
	v_add_u32_e32 v64, s43, v173
	ds_read_b128 v[66:69], v64
	ds_read_b128 v[70:73], v64 offset:1024
	ds_read_b128 v[74:77], v64 offset:2048
	ds_read_b128 v[78:81], v64 offset:3072
	v_add_u32_e32 v64, s48, v173
	ds_read_b128 v[146:149], v64
	ds_read_b128 v[150:153], v64 offset:1024
	ds_read_b128 v[166:169], v64 offset:2048
	ds_read_b128 v[176:179], v64 offset:3072
	s_add_u32 s26, s26, 0x40000
	s_addc_u32 s27, s27, 0
	s_mov_b32 m0, s39
	ds_read_b128 v[180:183], v175 offset:32768
	ds_read_b128 v[184:187], v175 offset:33792
	ds_read_b128 v[188:191], v175 offset:34816
	ds_read_b128 v[192:195], v175 offset:35840
	ds_read_b128 v[212:215], v175 offset:36864
	ds_read_b128 v[216:219], v175 offset:37888
	ds_read_b128 v[220:223], v175 offset:38912
	ds_read_b128 v[224:227], v175 offset:39936
	global_load_lds_dwordx4 v160, s[26:27]
	s_mov_b32 m0, s40
	s_nop 0
	global_load_lds_dwordx4 v156, s[26:27]
	s_waitcnt vmcnt(8)
	s_waitcnt lgkmcnt(0)
	s_barrier
	s_waitcnt lgkmcnt(0)
	v_mfma_f32_16x16x32_bf16 v[142:145], v[66:69], v[180:183], v[142:145]
	v_mfma_f32_16x16x32_bf16 v[138:141], v[74:77], v[180:183], v[138:141]
	v_mfma_f32_16x16x32_bf16 v[126:129], v[66:69], v[188:191], v[126:129]
	v_mfma_f32_16x16x32_bf16 v[122:125], v[74:77], v[188:191], v[122:125]
	v_mfma_f32_16x16x32_bf16 v[110:113], v[66:69], v[212:215], v[110:113]
	v_mfma_f32_16x16x32_bf16 v[106:109], v[74:77], v[212:215], v[106:109]
	v_mfma_f32_16x16x32_bf16 v[94:97], v[66:69], v[220:223], v[94:97]
	v_mfma_f32_16x16x32_bf16 v[90:93], v[74:77], v[220:223], v[90:93]
	v_mfma_f32_16x16x32_bf16 v[142:145], v[70:73], v[184:187], v[142:145]
	v_mfma_f32_16x16x32_bf16 v[138:141], v[78:81], v[184:187], v[138:141]
	v_mfma_f32_16x16x32_bf16 v[126:129], v[70:73], v[192:195], v[126:129]
	v_mfma_f32_16x16x32_bf16 v[122:125], v[78:81], v[192:195], v[122:125]
	v_mfma_f32_16x16x32_bf16 v[110:113], v[70:73], v[216:219], v[110:113]
	v_mfma_f32_16x16x32_bf16 v[106:109], v[78:81], v[216:219], v[106:109]
	v_mfma_f32_16x16x32_bf16 v[94:97], v[70:73], v[224:227], v[94:97]
	v_mfma_f32_16x16x32_bf16 v[90:93], v[78:81], v[224:227], v[90:93]
	v_mfma_f32_16x16x32_bf16 v[134:137], v[146:149], v[180:183], v[134:137]
	v_mfma_f32_16x16x32_bf16 v[130:133], v[166:169], v[180:183], v[130:133]
	v_mfma_f32_16x16x32_bf16 v[118:121], v[146:149], v[188:191], v[118:121]
	v_mfma_f32_16x16x32_bf16 v[114:117], v[166:169], v[188:191], v[114:117]
	v_mfma_f32_16x16x32_bf16 v[102:105], v[146:149], v[212:215], v[102:105]
	v_mfma_f32_16x16x32_bf16 v[98:101], v[166:169], v[212:215], v[98:101]
	v_mfma_f32_16x16x32_bf16 v[86:89], v[146:149], v[220:223], v[86:89]
	v_mfma_f32_16x16x32_bf16 v[82:85], v[166:169], v[220:223], v[82:85]
	v_mfma_f32_16x16x32_bf16 v[134:137], v[150:153], v[184:187], v[134:137]
	v_mfma_f32_16x16x32_bf16 v[130:133], v[176:179], v[184:187], v[130:133]
	v_mfma_f32_16x16x32_bf16 v[118:121], v[150:153], v[192:195], v[118:121]
	v_mfma_f32_16x16x32_bf16 v[114:117], v[176:179], v[192:195], v[114:117]
	v_mfma_f32_16x16x32_bf16 v[102:105], v[150:153], v[216:219], v[102:105]
	v_mfma_f32_16x16x32_bf16 v[98:101], v[176:179], v[216:219], v[98:101]
	v_mfma_f32_16x16x32_bf16 v[86:89], v[150:153], v[224:227], v[86:89]
	v_mfma_f32_16x16x32_bf16 v[82:85], v[176:179], v[224:227], v[82:85]
	s_barrier
	s_mov_b32 m0, s44
	s_add_u32 s100, s4, s68
	s_addc_u32 s101, s5, s69
	s_add_u32 s4, s4, 0x40080
	ds_read_b128 v[180:183], v175 offset:49152
	ds_read_b128 v[184:187], v175 offset:50176
	ds_read_b128 v[188:191], v175 offset:51200
	ds_read_b128 v[192:195], v175 offset:52224
	ds_read_b128 v[212:215], v175 offset:53248
	ds_read_b128 v[216:219], v175 offset:54272
	ds_read_b128 v[220:223], v175 offset:55296
	ds_read_b128 v[224:227], v175 offset:56320
	global_load_lds_dwordx4 v158, s[100:101]
	s_mov_b32 m0, s45
	s_addc_u32 s5, s5, 0
	global_load_lds_dwordx4 v154, s[100:101]
	s_mov_b32 m0, s49
	s_add_u32 s100, s26, s68
	global_load_lds_dwordx4 v158, s[4:5]
	s_addc_u32 s101, s27, s69
	s_mov_b32 m0, s50
	s_sub_u32 s100, s100, 0x40000
	global_load_lds_dwordx4 v154, s[4:5]
	s_subb_u32 s101, s101, 0
	s_mov_b32 m0, s46
	s_nop 0
	global_load_lds_dwordx4 v160, s[100:101]
	s_mov_b32 m0, s47
	s_nop 0
	global_load_lds_dwordx4 v156, s[100:101]
	s_waitcnt vmcnt(8)
	s_waitcnt lgkmcnt(0)
	s_barrier
	s_waitcnt lgkmcnt(0)
	v_mfma_f32_16x16x32_bf16 v[60:63], v[66:69], v[180:183], v[60:63]
	v_mfma_f32_16x16x32_bf16 v[56:59], v[74:77], v[180:183], v[56:59]
	v_mfma_f32_16x16x32_bf16 v[44:47], v[66:69], v[188:191], v[44:47]
	v_mfma_f32_16x16x32_bf16 v[40:43], v[74:77], v[188:191], v[40:43]
	v_mfma_f32_16x16x32_bf16 v[28:31], v[66:69], v[212:215], v[28:31]
	v_mfma_f32_16x16x32_bf16 v[24:27], v[74:77], v[212:215], v[24:27]
	v_mfma_f32_16x16x32_bf16 v[12:15], v[66:69], v[220:223], v[12:15]
	v_mfma_f32_16x16x32_bf16 v[8:11], v[74:77], v[220:223], v[8:11]
	v_mfma_f32_16x16x32_bf16 v[60:63], v[70:73], v[184:187], v[60:63]
	v_mfma_f32_16x16x32_bf16 v[56:59], v[78:81], v[184:187], v[56:59]
	v_mfma_f32_16x16x32_bf16 v[44:47], v[70:73], v[192:195], v[44:47]
	v_mfma_f32_16x16x32_bf16 v[40:43], v[78:81], v[192:195], v[40:43]
	v_mfma_f32_16x16x32_bf16 v[28:31], v[70:73], v[216:219], v[28:31]
	v_mfma_f32_16x16x32_bf16 v[24:27], v[78:81], v[216:219], v[24:27]
	v_mfma_f32_16x16x32_bf16 v[12:15], v[70:73], v[224:227], v[12:15]
	v_mfma_f32_16x16x32_bf16 v[8:11], v[78:81], v[224:227], v[8:11]
	v_mfma_f32_16x16x32_bf16 v[52:55], v[146:149], v[180:183], v[52:55]
	v_mfma_f32_16x16x32_bf16 v[48:51], v[166:169], v[180:183], v[48:51]
	v_mfma_f32_16x16x32_bf16 v[36:39], v[146:149], v[188:191], v[36:39]
	v_mfma_f32_16x16x32_bf16 v[32:35], v[166:169], v[188:191], v[32:35]
	v_mfma_f32_16x16x32_bf16 v[20:23], v[146:149], v[212:215], v[20:23]
	v_mfma_f32_16x16x32_bf16 v[16:19], v[166:169], v[212:215], v[16:19]
	v_mfma_f32_16x16x32_bf16 v[4:7], v[146:149], v[220:223], v[4:7]
	v_mfma_f32_16x16x32_bf16 v[0:3], v[166:169], v[220:223], v[0:3]
	v_mfma_f32_16x16x32_bf16 v[52:55], v[150:153], v[184:187], v[52:55]
	v_mfma_f32_16x16x32_bf16 v[48:51], v[176:179], v[184:187], v[48:51]
	v_mfma_f32_16x16x32_bf16 v[36:39], v[150:153], v[192:195], v[36:39]
	v_mfma_f32_16x16x32_bf16 v[32:35], v[176:179], v[192:195], v[32:35]
	v_mfma_f32_16x16x32_bf16 v[20:23], v[150:153], v[216:219], v[20:23]
	v_mfma_f32_16x16x32_bf16 v[16:19], v[176:179], v[216:219], v[16:19]
	v_mfma_f32_16x16x32_bf16 v[4:7], v[150:153], v[224:227], v[4:7]
	v_mfma_f32_16x16x32_bf16 v[0:3], v[176:179], v[224:227], v[0:3]
	s_barrier
	s_add_i32 s61, s61, 2
	s_add_u32 s0, s0, 0x100
	s_addc_u32 s1, s1, 0
	s_add_u32 s59, s59, 0x100
	s_addc_u32 s60, s60, 0
	s_cmp_gt_u32 s61, 13
	s_cbranch_scc0 .LBB0_814
	s_and_b64 vcc, exec, s[20:21]
	s_cbranch_vccz .LBB0_817
	s_barrier

.LBB0_1400:
	s_waitcnt vmcnt(8)
	s_waitcnt lgkmcnt(0)
	s_not_b64 s[2:3], s[24:25]
	s_andn2_b64 vcc, exec, s[24:25]
	s_barrier
	s_cbranch_vccnz .LBB0_1402
	s_waitcnt lgkmcnt(0)
	v_mfma_f32_16x16x128_f8f6f4 v[192:195], v[16:23], v[56:63], v[192:195]
	v_mfma_f32_16x16x128_f8f6f4 v[184:187], v[24:31], v[56:63], v[184:187]
	v_mfma_f32_16x16x128_f8f6f4 v[176:179], v[16:23], v[48:55], v[176:179]
	v_mfma_f32_16x16x128_f8f6f4 v[168:171], v[24:31], v[48:55], v[168:171]
	v_mfma_f32_16x16x128_f8f6f4 v[160:163], v[16:23], v[40:47], v[160:163]
	v_mfma_f32_16x16x128_f8f6f4 v[152:155], v[24:31], v[40:47], v[152:155]
	v_mfma_f32_16x16x128_f8f6f4 v[144:147], v[16:23], v[32:39], v[144:147]
	v_mfma_f32_16x16x128_f8f6f4 v[136:139], v[24:31], v[32:39], v[136:139]
	v_mfma_f32_16x16x128_f8f6f4 v[188:191], v[0:7], v[56:63], v[188:191]
	v_mfma_f32_16x16x128_f8f6f4 v[180:183], v[8:15], v[56:63], v[180:183]
	v_mfma_f32_16x16x128_f8f6f4 v[172:175], v[0:7], v[48:55], v[172:175]
	v_mfma_f32_16x16x128_f8f6f4 v[164:167], v[8:15], v[48:55], v[164:167]
	v_mfma_f32_16x16x128_f8f6f4 v[156:159], v[0:7], v[40:47], v[156:159]
	v_mfma_f32_16x16x128_f8f6f4 v[148:151], v[8:15], v[40:47], v[148:151]
	v_mfma_f32_16x16x128_f8f6f4 v[140:143], v[0:7], v[32:39], v[140:143]
	v_mfma_f32_16x16x128_f8f6f4 v[132:135], v[8:15], v[32:39], v[132:135]
.LBB0_1402:
	s_add_u32 s28, s26, 0x80
	s_addc_u32 s29, s27, 0
	s_and_b64 s[0:1], s[0:1], exec
	v_readlane_b32 s0, v242, 53
	v_readlane_b32 s1, v242, 54
	s_cselect_b32 s29, s1, s29
	s_cselect_b32 s28, s0, s28
	s_cselect_b32 s31, s15, s66
	s_cselect_b32 s30, s64, s65
	s_barrier
	s_mov_b32 m0, s42
	s_waitcnt lgkmcnt(0)
	ds_read_b128 v[56:59], v218 offset:16384
	ds_read_b128 v[60:63], v218 offset:17408
	ds_read_b128 v[48:51], v218 offset:18432
	ds_read_b128 v[52:55], v218 offset:19456
	ds_read_b128 v[40:43], v218 offset:20480
	ds_read_b128 v[44:47], v218 offset:21504
	ds_read_b128 v[32:35], v218 offset:22528
	ds_read_b128 v[36:39], v218 offset:23552
	s_add_u32 s0, s30, 0x20000
	global_load_lds_dwordx4 v211, s[30:31]
	s_mov_b32 m0, s43
	s_addc_u32 s1, s31, 0
	global_load_lds_dwordx4 v212, s[30:31]
	s_mov_b32 m0, s45
	s_andn2_b64 vcc, exec, s[22:23]
	global_load_lds_dwordx4 v211, s[0:1]
	s_mov_b32 m0, s46
	s_nop 0
	global_load_lds_dwordx4 v212, s[0:1]
	s_mov_b32 m0, s19
	s_nop 0
	global_load_lds_dwordx4 v213, s[28:29]
	s_mov_b32 m0, s47
	s_nop 0
	global_load_lds_dwordx4 v215, s[28:29]
	s_waitcnt vmcnt(8)
	s_waitcnt lgkmcnt(0)
	s_not_b64 s[0:1], s[22:23]
	s_barrier
	s_cbranch_vccnz .LBB0_1404
	s_waitcnt lgkmcnt(0)
	v_mfma_f32_16x16x128_f8f6f4 v[128:131], v[16:23], v[56:63], v[128:131]
	v_mfma_f32_16x16x128_f8f6f4 v[120:123], v[24:31], v[56:63], v[120:123]
	v_mfma_f32_16x16x128_f8f6f4 v[112:115], v[16:23], v[48:55], v[112:115]
	v_mfma_f32_16x16x128_f8f6f4 v[104:107], v[24:31], v[48:55], v[104:107]
	v_mfma_f32_16x16x128_f8f6f4 v[96:99], v[16:23], v[40:47], v[96:99]
	v_mfma_f32_16x16x128_f8f6f4 v[88:91], v[24:31], v[40:47], v[88:91]
	v_mfma_f32_16x16x128_f8f6f4 v[80:83], v[16:23], v[32:39], v[80:83]
	v_mfma_f32_16x16x128_f8f6f4 v[72:75], v[24:31], v[32:39], v[72:75]
	v_mfma_f32_16x16x128_f8f6f4 v[124:127], v[0:7], v[56:63], v[124:127]
	v_mfma_f32_16x16x128_f8f6f4 v[116:119], v[8:15], v[56:63], v[116:119]
	v_mfma_f32_16x16x128_f8f6f4 v[108:111], v[0:7], v[48:55], v[108:111]
	v_mfma_f32_16x16x128_f8f6f4 v[100:103], v[8:15], v[48:55], v[100:103]
	v_mfma_f32_16x16x128_f8f6f4 v[92:95], v[0:7], v[40:47], v[92:95]
	v_mfma_f32_16x16x128_f8f6f4 v[84:87], v[8:15], v[40:47], v[84:87]
	v_mfma_f32_16x16x128_f8f6f4 v[76:79], v[0:7], v[32:39], v[76:79]
	v_mfma_f32_16x16x128_f8f6f4 v[68:71], v[8:15], v[32:39], v[68:71]
.LBB0_1404:
	s_barrier
	v_add_u32_e32 v0, s52, v217
	v_add_u32_e32 v12, s57, v217
	ds_read_b128 v[16:19], v0
	ds_read_b128 v[20:23], v0 offset:1024
	ds_read_b128 v[24:27], v0 offset:2048
	ds_read_b128 v[28:31], v0 offset:3072
	ds_read_b128 v[0:3], v12
	ds_read_b128 v[4:7], v12 offset:1024
	ds_read_b128 v[8:11], v12 offset:2048
	ds_read_b128 v[12:15], v12 offset:3072
	s_mov_b32 m0, s48
	ds_read_b128 v[56:59], v218 offset:32768
	ds_read_b128 v[60:63], v218 offset:33792
	ds_read_b128 v[48:51], v218 offset:34816
	ds_read_b128 v[52:55], v218 offset:35840
	ds_read_b128 v[40:43], v218 offset:36864
	ds_read_b128 v[44:47], v218 offset:37888
	ds_read_b128 v[32:35], v218 offset:38912
	ds_read_b128 v[36:39], v218 offset:39936
	s_and_b64 vcc, exec, s[2:3]
	global_load_lds_dwordx4 v214, s[28:29]
	s_mov_b32 m0, s49
	s_nop 0
	global_load_lds_dwordx4 v216, s[28:29]
	s_waitcnt vmcnt(8)
	s_waitcnt lgkmcnt(0)
	s_barrier
	s_cbranch_vccnz .LBB0_1406
	s_waitcnt lgkmcnt(0)
	v_mfma_f32_16x16x128_f8f6f4 v[192:195], v[16:23], v[56:63], v[192:195]
	v_mfma_f32_16x16x128_f8f6f4 v[184:187], v[24:31], v[56:63], v[184:187]
	v_mfma_f32_16x16x128_f8f6f4 v[176:179], v[16:23], v[48:55], v[176:179]
	v_mfma_f32_16x16x128_f8f6f4 v[168:171], v[24:31], v[48:55], v[168:171]
	v_mfma_f32_16x16x128_f8f6f4 v[160:163], v[16:23], v[40:47], v[160:163]
	v_mfma_f32_16x16x128_f8f6f4 v[152:155], v[24:31], v[40:47], v[152:155]
	v_mfma_f32_16x16x128_f8f6f4 v[144:147], v[16:23], v[32:39], v[144:147]
	v_mfma_f32_16x16x128_f8f6f4 v[136:139], v[24:31], v[32:39], v[136:139]
	v_mfma_f32_16x16x128_f8f6f4 v[188:191], v[0:7], v[56:63], v[188:191]
	v_mfma_f32_16x16x128_f8f6f4 v[180:183], v[8:15], v[56:63], v[180:183]
	v_mfma_f32_16x16x128_f8f6f4 v[172:175], v[0:7], v[48:55], v[172:175]
	v_mfma_f32_16x16x128_f8f6f4 v[164:167], v[8:15], v[48:55], v[164:167]
	v_mfma_f32_16x16x128_f8f6f4 v[156:159], v[0:7], v[40:47], v[156:159]
	v_mfma_f32_16x16x128_f8f6f4 v[148:151], v[8:15], v[40:47], v[148:151]
	v_mfma_f32_16x16x128_f8f6f4 v[140:143], v[0:7], v[32:39], v[140:143]
	v_mfma_f32_16x16x128_f8f6f4 v[132:135], v[8:15], v[32:39], v[132:135]
.LBB0_1406:
	s_barrier
	s_waitcnt lgkmcnt(0)
	ds_read_b128 v[56:59], v218 offset:49152
	ds_read_b128 v[60:63], v218 offset:50176
	ds_read_b128 v[48:51], v218 offset:51200
	ds_read_b128 v[52:55], v218 offset:52224
	ds_read_b128 v[40:43], v218 offset:53248
	ds_read_b128 v[44:47], v218 offset:54272
	ds_read_b128 v[32:35], v218 offset:55296
	ds_read_b128 v[36:39], v218 offset:56320
	s_add_u32 s100, s30, s68
	s_addc_u32 s101, s31, s69
	s_mov_b32 m0, s53
	s_add_u32 s2, s30, 0x20080
	global_load_lds_dwordx4 v211, s[100:101]
	s_mov_b32 m0, s54
	s_addc_u32 s3, s31, 0
	global_load_lds_dwordx4 v212, s[100:101]
	s_mov_b32 m0, s58
	s_and_b64 vcc, exec, s[0:1]
	global_load_lds_dwordx4 v211, s[2:3]
	s_mov_b32 m0, s59
	s_add_u32 s100, s28, s68
	global_load_lds_dwordx4 v212, s[2:3]
	s_addc_u32 s101, s29, s69
	s_mov_b32 m0, s55
	s_nop 0
	global_load_lds_dwordx4 v213, s[100:101]
	s_mov_b32 m0, s56
	s_nop 0
	global_load_lds_dwordx4 v215, s[100:101]
	s_waitcnt vmcnt(8)
	s_waitcnt lgkmcnt(0)
	s_barrier
	s_cbranch_vccnz .LBB0_1397
	s_waitcnt lgkmcnt(0)
	v_mfma_f32_16x16x128_f8f6f4 v[128:131], v[16:23], v[56:63], v[128:131]
	v_mfma_f32_16x16x128_f8f6f4 v[120:123], v[24:31], v[56:63], v[120:123]
	v_mfma_f32_16x16x128_f8f6f4 v[112:115], v[16:23], v[48:55], v[112:115]
	v_mfma_f32_16x16x128_f8f6f4 v[104:107], v[24:31], v[48:55], v[104:107]
	v_mfma_f32_16x16x128_f8f6f4 v[96:99], v[16:23], v[40:47], v[96:99]
	v_mfma_f32_16x16x128_f8f6f4 v[88:91], v[24:31], v[40:47], v[88:91]
	v_mfma_f32_16x16x128_f8f6f4 v[80:83], v[16:23], v[32:39], v[80:83]
	v_mfma_f32_16x16x128_f8f6f4 v[72:75], v[24:31], v[32:39], v[72:75]
	v_mfma_f32_16x16x128_f8f6f4 v[124:127], v[0:7], v[56:63], v[124:127]
	v_mfma_f32_16x16x128_f8f6f4 v[116:119], v[8:15], v[56:63], v[116:119]
	v_mfma_f32_16x16x128_f8f6f4 v[108:111], v[0:7], v[48:55], v[108:111]
	v_mfma_f32_16x16x128_f8f6f4 v[100:103], v[8:15], v[48:55], v[100:103]
	v_mfma_f32_16x16x128_f8f6f4 v[92:95], v[0:7], v[40:47], v[92:95]
	v_mfma_f32_16x16x128_f8f6f4 v[84:87], v[8:15], v[40:47], v[84:87]
	v_mfma_f32_16x16x128_f8f6f4 v[76:79], v[0:7], v[32:39], v[76:79]
	v_mfma_f32_16x16x128_f8f6f4 v[68:71], v[8:15], v[32:39], v[68:71]
	s_branch .LBB0_1397

.LBB0_1476:
	v_add_u32_e32 v0, s23, v215
	v_add_u32_e32 v12, s43, v215
	ds_read_b128 v[16:19], v0
	ds_read_b128 v[20:23], v0 offset:1024
	ds_read_b128 v[24:27], v0 offset:2048
	ds_read_b128 v[28:31], v0 offset:3072
	ds_read_b128 v[0:3], v12
	ds_read_b128 v[4:7], v12 offset:1024
	ds_read_b128 v[8:11], v12 offset:2048
	ds_read_b128 v[12:15], v12 offset:3072
	ds_read_b128 v[56:59], v216
	ds_read_b128 v[60:63], v216 offset:1024
	ds_read_b128 v[48:51], v216 offset:2048
	ds_read_b128 v[52:55], v216 offset:3072
	ds_read_b128 v[40:43], v216 offset:4096
	ds_read_b128 v[44:47], v216 offset:5120
	ds_read_b128 v[32:35], v216 offset:6144
	ds_read_b128 v[36:39], v216 offset:7168
	s_add_i32 m0, s46, 0xc000
	s_andn2_b64 vcc, exec, s[28:29]
	global_load_lds_dwordx4 v212, s[30:31]
	s_add_i32 m0, s46, 0xe000
	s_nop 0
	global_load_lds_dwordx4 v214, s[30:31]
	s_waitcnt vmcnt(8)
	s_waitcnt lgkmcnt(0)
	s_not_b64 s[2:3], s[28:29]
	s_barrier
	s_cbranch_vccnz .LBB0_1478
	s_waitcnt lgkmcnt(0)
	v_mfma_f32_16x16x128_f8f6f4 v[192:195], v[16:23], v[56:63], v[192:195]
	v_mfma_f32_16x16x128_f8f6f4 v[188:191], v[24:31], v[56:63], v[188:191]
	v_mfma_f32_16x16x128_f8f6f4 v[176:179], v[16:23], v[48:55], v[176:179]
	v_mfma_f32_16x16x128_f8f6f4 v[172:175], v[24:31], v[48:55], v[172:175]
	v_mfma_f32_16x16x128_f8f6f4 v[160:163], v[16:23], v[40:47], v[160:163]
	v_mfma_f32_16x16x128_f8f6f4 v[156:159], v[24:31], v[40:47], v[156:159]
	v_mfma_f32_16x16x128_f8f6f4 v[144:147], v[16:23], v[32:39], v[144:147]
	v_mfma_f32_16x16x128_f8f6f4 v[140:143], v[24:31], v[32:39], v[140:143]
	v_mfma_f32_16x16x128_f8f6f4 v[184:187], v[0:7], v[56:63], v[184:187]
	v_mfma_f32_16x16x128_f8f6f4 v[180:183], v[8:15], v[56:63], v[180:183]
	v_mfma_f32_16x16x128_f8f6f4 v[168:171], v[0:7], v[48:55], v[168:171]
	v_mfma_f32_16x16x128_f8f6f4 v[164:167], v[8:15], v[48:55], v[164:167]
	v_mfma_f32_16x16x128_f8f6f4 v[152:155], v[0:7], v[40:47], v[152:155]
	v_mfma_f32_16x16x128_f8f6f4 v[148:151], v[8:15], v[40:47], v[148:151]
	v_mfma_f32_16x16x128_f8f6f4 v[136:139], v[0:7], v[32:39], v[136:139]
	v_mfma_f32_16x16x128_f8f6f4 v[132:135], v[8:15], v[32:39], v[132:135]
.LBB0_1478:
	s_add_u32 s0, s30, 0xfffc0080
	s_addc_u32 s1, s31, -1
	s_cmp_eq_u32 s65, 12
	s_cselect_b32 s35, s13, s1
	s_cselect_b32 s34, s62, s0
	s_cselect_b32 s37, s15, s64
	s_cselect_b32 s36, s61, s63
	s_barrier
	s_mov_b32 m0, s25
	s_waitcnt lgkmcnt(0)
	ds_read_b128 v[56:59], v216 offset:16384
	ds_read_b128 v[60:63], v216 offset:17408
	ds_read_b128 v[48:51], v216 offset:18432
	ds_read_b128 v[52:55], v216 offset:19456
	ds_read_b128 v[40:43], v216 offset:20480
	ds_read_b128 v[44:47], v216 offset:21504
	ds_read_b128 v[32:35], v216 offset:22528
	ds_read_b128 v[36:39], v216 offset:23552
	s_add_u32 s0, s36, 0x40000
	global_load_lds_dwordx4 v211, s[36:37]
	s_mov_b32 m0, s42
	s_addc_u32 s1, s37, 0
	global_load_lds_dwordx4 v213, s[36:37]
	s_mov_b32 m0, s44
	s_andn2_b64 vcc, exec, s[26:27]
	global_load_lds_dwordx4 v211, s[0:1]
	s_mov_b32 m0, s45
	s_nop 0
	global_load_lds_dwordx4 v213, s[0:1]
	s_mov_b32 m0, s46
	s_nop 0
	global_load_lds_dwordx4 v212, s[34:35]
	s_mov_b32 m0, s47
	s_nop 0
	global_load_lds_dwordx4 v214, s[34:35]
	s_waitcnt vmcnt(8)
	s_waitcnt lgkmcnt(0)
	s_not_b64 s[0:1], s[26:27]
	s_barrier
	s_cbranch_vccnz .LBB0_1480
	s_waitcnt lgkmcnt(0)
	v_mfma_f32_16x16x128_f8f6f4 v[128:131], v[16:23], v[56:63], v[128:131]
	v_mfma_f32_16x16x128_f8f6f4 v[124:127], v[24:31], v[56:63], v[124:127]
	v_mfma_f32_16x16x128_f8f6f4 v[112:115], v[16:23], v[48:55], v[112:115]
	v_mfma_f32_16x16x128_f8f6f4 v[108:111], v[24:31], v[48:55], v[108:111]
	v_mfma_f32_16x16x128_f8f6f4 v[96:99], v[16:23], v[40:47], v[96:99]
	v_mfma_f32_16x16x128_f8f6f4 v[92:95], v[24:31], v[40:47], v[92:95]
	v_mfma_f32_16x16x128_f8f6f4 v[80:83], v[16:23], v[32:39], v[80:83]
	v_mfma_f32_16x16x128_f8f6f4 v[76:79], v[24:31], v[32:39], v[76:79]
	v_mfma_f32_16x16x128_f8f6f4 v[120:123], v[0:7], v[56:63], v[120:123]
	v_mfma_f32_16x16x128_f8f6f4 v[116:119], v[8:15], v[56:63], v[116:119]
	v_mfma_f32_16x16x128_f8f6f4 v[104:107], v[0:7], v[48:55], v[104:107]
	v_mfma_f32_16x16x128_f8f6f4 v[100:103], v[8:15], v[48:55], v[100:103]
	v_mfma_f32_16x16x128_f8f6f4 v[88:91], v[0:7], v[40:47], v[88:91]
	v_mfma_f32_16x16x128_f8f6f4 v[84:87], v[8:15], v[40:47], v[84:87]
	v_mfma_f32_16x16x128_f8f6f4 v[72:75], v[0:7], v[32:39], v[72:75]
	v_mfma_f32_16x16x128_f8f6f4 v[68:71], v[8:15], v[32:39], v[68:71]
.LBB0_1480:
	s_barrier
	v_add_u32_e32 v0, s52, v215
	v_add_u32_e32 v12, s57, v215
	ds_read_b128 v[16:19], v0
	ds_read_b128 v[20:23], v0 offset:1024
	ds_read_b128 v[24:27], v0 offset:2048
	ds_read_b128 v[28:31], v0 offset:3072
	ds_read_b128 v[0:3], v12
	ds_read_b128 v[4:7], v12 offset:1024
	ds_read_b128 v[8:11], v12 offset:2048
	ds_read_b128 v[12:15], v12 offset:3072
	s_add_u32 s66, s34, 0x40000
	s_mov_b32 m0, s48
	ds_read_b128 v[56:59], v216 offset:32768
	ds_read_b128 v[60:63], v216 offset:33792
	ds_read_b128 v[48:51], v216 offset:34816
	ds_read_b128 v[52:55], v216 offset:35840
	ds_read_b128 v[40:43], v216 offset:36864
	ds_read_b128 v[44:47], v216 offset:37888
	ds_read_b128 v[32:35], v216 offset:38912
	ds_read_b128 v[36:39], v216 offset:39936
	s_addc_u32 s67, s35, 0
	s_and_b64 vcc, exec, s[2:3]
	global_load_lds_dwordx4 v212, s[66:67]
	s_mov_b32 m0, s49
	s_nop 0
	global_load_lds_dwordx4 v214, s[66:67]
	s_waitcnt vmcnt(8)
	s_waitcnt lgkmcnt(0)
	s_barrier
	s_cbranch_vccnz .LBB0_1482
	s_waitcnt lgkmcnt(0)
	v_mfma_f32_16x16x128_f8f6f4 v[192:195], v[16:23], v[56:63], v[192:195]
	v_mfma_f32_16x16x128_f8f6f4 v[188:191], v[24:31], v[56:63], v[188:191]
	v_mfma_f32_16x16x128_f8f6f4 v[176:179], v[16:23], v[48:55], v[176:179]
	v_mfma_f32_16x16x128_f8f6f4 v[172:175], v[24:31], v[48:55], v[172:175]
	v_mfma_f32_16x16x128_f8f6f4 v[160:163], v[16:23], v[40:47], v[160:163]
	v_mfma_f32_16x16x128_f8f6f4 v[156:159], v[24:31], v[40:47], v[156:159]
	v_mfma_f32_16x16x128_f8f6f4 v[144:147], v[16:23], v[32:39], v[144:147]
	v_mfma_f32_16x16x128_f8f6f4 v[140:143], v[24:31], v[32:39], v[140:143]
	v_mfma_f32_16x16x128_f8f6f4 v[184:187], v[0:7], v[56:63], v[184:187]
	v_mfma_f32_16x16x128_f8f6f4 v[180:183], v[8:15], v[56:63], v[180:183]
	v_mfma_f32_16x16x128_f8f6f4 v[168:171], v[0:7], v[48:55], v[168:171]
	v_mfma_f32_16x16x128_f8f6f4 v[164:167], v[8:15], v[48:55], v[164:167]
	v_mfma_f32_16x16x128_f8f6f4 v[152:155], v[0:7], v[40:47], v[152:155]
	v_mfma_f32_16x16x128_f8f6f4 v[148:151], v[8:15], v[40:47], v[148:151]
	v_mfma_f32_16x16x128_f8f6f4 v[136:139], v[0:7], v[32:39], v[136:139]
	v_mfma_f32_16x16x128_f8f6f4 v[132:135], v[8:15], v[32:39], v[132:135]
.LBB0_1482:
	s_barrier
	s_waitcnt lgkmcnt(0)
	ds_read_b128 v[56:59], v216 offset:49152
	ds_read_b128 v[60:63], v216 offset:50176
	ds_read_b128 v[48:51], v216 offset:51200
	ds_read_b128 v[52:55], v216 offset:52224
	ds_read_b128 v[40:43], v216 offset:53248
	ds_read_b128 v[44:47], v216 offset:54272
	ds_read_b128 v[32:35], v216 offset:55296
	ds_read_b128 v[36:39], v216 offset:56320
	s_add_u32 s100, s36, s68
	s_addc_u32 s101, s37, s69
	s_mov_b32 m0, s53
	s_add_u32 s2, s36, 0x40080
	global_load_lds_dwordx4 v211, s[100:101]
	s_mov_b32 m0, s54
	s_addc_u32 s3, s37, 0
	global_load_lds_dwordx4 v213, s[100:101]
	s_mov_b32 m0, s58
	s_and_b64 vcc, exec, s[0:1]
	global_load_lds_dwordx4 v211, s[2:3]
	s_mov_b32 m0, s59
	s_add_u32 s100, s34, s68
	global_load_lds_dwordx4 v213, s[2:3]
	s_addc_u32 s101, s35, s69
	s_mov_b32 m0, s55
	s_nop 0
	global_load_lds_dwordx4 v212, s[100:101]
	s_mov_b32 m0, s56
	s_nop 0
	global_load_lds_dwordx4 v214, s[100:101]
	s_waitcnt vmcnt(8)
	s_waitcnt lgkmcnt(0)
	s_barrier
	s_cbranch_vccnz .LBB0_1475
	s_waitcnt lgkmcnt(0)
	v_mfma_f32_16x16x128_f8f6f4 v[128:131], v[16:23], v[56:63], v[128:131]
	v_mfma_f32_16x16x128_f8f6f4 v[124:127], v[24:31], v[56:63], v[124:127]
	v_mfma_f32_16x16x128_f8f6f4 v[112:115], v[16:23], v[48:55], v[112:115]
	v_mfma_f32_16x16x128_f8f6f4 v[108:111], v[24:31], v[48:55], v[108:111]
	v_mfma_f32_16x16x128_f8f6f4 v[96:99], v[16:23], v[40:47], v[96:99]
	v_mfma_f32_16x16x128_f8f6f4 v[92:95], v[24:31], v[40:47], v[92:95]
	v_mfma_f32_16x16x128_f8f6f4 v[80:83], v[16:23], v[32:39], v[80:83]
	v_mfma_f32_16x16x128_f8f6f4 v[76:79], v[24:31], v[32:39], v[76:79]
	v_mfma_f32_16x16x128_f8f6f4 v[120:123], v[0:7], v[56:63], v[120:123]
	v_mfma_f32_16x16x128_f8f6f4 v[116:119], v[8:15], v[56:63], v[116:119]
	v_mfma_f32_16x16x128_f8f6f4 v[104:107], v[0:7], v[48:55], v[104:107]
	v_mfma_f32_16x16x128_f8f6f4 v[100:103], v[8:15], v[48:55], v[100:103]
	v_mfma_f32_16x16x128_f8f6f4 v[88:91], v[0:7], v[40:47], v[88:91]
	v_mfma_f32_16x16x128_f8f6f4 v[84:87], v[8:15], v[40:47], v[84:87]
	v_mfma_f32_16x16x128_f8f6f4 v[72:75], v[0:7], v[32:39], v[72:75]
	v_mfma_f32_16x16x128_f8f6f4 v[68:71], v[8:15], v[32:39], v[68:71]
	s_branch .LBB0_1475
